# lever 4: one static s_setprio 1 for waves 0-3 (kernel entry, restored after the recurrence phase), per-cluster priority flips in the GEMM loops deleted
# speedup vs baseline: 1.0052x; 1.0052x over previous
; __device__ __forceinline__ int lane_id() { int l; asm volatile("v_mbcnt_lo_u32_b32 %0, -1, 0\n\tv_mbcnt_hi_u32_b32 %0, -1, %0" : "=v"(l)); return l; }
; #define PG8_LAS __attribute__((address_space(3)))
; __global__ void __launch_bounds__(NT, 2) fwd_kernel(Params p) {
;     extern __shared__ __attribute__((aligned(16))) char lds[];
;     const int WID_ = __builtin_amdgcn_readfirstlane((int)(threadIdx.x >> 6));
;     cg::grid_group grid = cg::this_grid();
;     PG8_LAS unsigned char* ldsl = (PG8_LAS unsigned char*)lds;
;     char* ws = p.ws; char* dout = (char*)p.out; float* out = p.out;
;     ...
;     volatile __attribute__((address_space(3))) unsigned* bst = (volatile __attribute__((address_space(3))) unsigned*)(ldsl + LDS_BYTES - 64);
;     if (WID_ == 0 && lane_id() < 2) bst[lane_id()] = 0u;
;     __syncthreads();
;     const XcdBarrier xbar = xcd_barrier_post(WID_, (unsigned*)(ws + W_CTL * MiB), bst);
_ZN12_GLOBAL__N_110fwd_kernelENS_6ParamsE:
	s_load_dword s3, s[0:1], 0x160
	v_and_b32_e32 v1, 0x3ff, v0
	s_add_u32 s20, s0, 0x158
	v_readfirstlane_b32 s22, v1
	s_addc_u32 s21, s1, 0
	s_load_dwordx8 s[88:95], s[0:1], 0x140
	s_cmp_lt_u32 s22, 64
	s_waitcnt lgkmcnt(0)
	v_writelane_b32 v243, s3, 0
	s_cselect_b64 s[4:5], -1, 0
	v_writelane_b32 v243, s4, 1
	s_cmp_gt_u32 s22, 63
	s_nop 0
	v_writelane_b32 v243, s5, 2
	s_cselect_b64 s[4:5], -1, 0
	s_cmp_lt_u32 s22, 256
	s_cbranch_scc0 .Lprio_k0
	s_setprio 1

; __device__ __forceinline__ void phase2(const int WID_, const char* items, float* Y, char* lds, const int vblk, const int nvblk) {
;     ...
;         if (upd) __builtin_amdgcn_s_setprio(3);
;         for (int c = 0; c < S / 64; c += 8) {
;             P2_STEP(1, c); P2_STEP(2, c + 1); P2_STEP(3, c + 2); P2_STEP(4, c + 3); P2_STEP(5, c + 4); P2_STEP(6, c + 5); P2_STEP(7, c + 6); P2_STEP(0, c + 7);
;         }
;         __builtin_amdgcn_s_setprio(0);
.LBB0_1606:
	s_setprio 0
	v_readlane_b32 s98, v243, 44
	s_nop 3
	s_cmp_gt_u32 s98, 3
	s_cbranch_scc1 .Lprio_pa
	s_setprio 1
